# nt cache policy on the in-projection (Z) epilogue stores
# speedup vs baseline: 1.1187x; 1.1187x over previous
; __device__ __forceinline__ unsigned cvt_pk_bf16(float lo, float hi) { unsigned r; asm volatile("v_cvt_pk_bf16_f32 %0, %1, %2" : "=v"(r) : "v"(lo), "v"(hi)); return r; }
;     __device__ __forceinline__ void operator()(const f32x4 (&acc)[2][2][4][2], const Unit& u, int wr, int wc, int fr, int fq) const {
;     ...
;         const int row0 = u.pm * BM + wr * 64 + fr; const int col0 = u.pn * BM + wc * 32 + 8 * fq; const bool sg = u.pn >= sig_pn;
; #pragma unroll
;         for (int ai = 0; ai < 2; ++ai)
; #pragma unroll
;             for (int m = 0; m < 4; ++m) { bf16* rowp = O + (size_t)(row0 + ai * HALF + m * 16) * ldc + col0;
; #pragma unroll
;                 for (int bj = 0; bj < 2; ++bj) { f32x4 v0 = acc[ai][bj][m][0], v1 = acc[ai][bj][m][1];
;                     if (sg) {
; #pragma unroll
;                         for (int j = 0; j < 4; ++j) { v0[j] = 1.0f + __expf(-v0[j]); v1[j] = 1.0f + __expf(-v1[j]); } }
;                     u32x4 w; w.x = cvt_pk_bf16(v0[0], v0[1]); w.y = cvt_pk_bf16(v0[2], v0[3]); w.z = cvt_pk_bf16(v1[0], v1[1]); w.w = cvt_pk_bf16(v1[2], v1[3]);
;                     *(u32x4*)(rowp + bj * HALF) = w; } }
.LBB0_224:
	v_lshl_add_u32 v148, s48, 8, v144
	v_lshl_or_b32 v140, s38, 8, v146
	v_mov_b64_e32 v[142:143], s[2:3]
	v_ashrrev_i32_e32 v141, 31, v140
	v_mad_i64_i32 v[142:143], s[8:9], v148, s33, v[142:143]
	v_cvt_pk_bf16_f32 v126, v126, v127
	v_cvt_pk_bf16_f32 v127, v128, v129
	v_cvt_pk_bf16_f32 v128, v122, v123
	v_cndmask_b32_e64 v122, 0, 1, s[50:51]
	v_lshl_add_u64 v[142:143], v[140:141], 1, v[142:143]
	v_cmp_ne_u32_e64 s[38:39], 1, v122
	s_andn2_b64 vcc, exec, s[50:51]
	v_cvt_pk_bf16_f32 v129, v124, v125
	flat_store_dwordx4 v[142:143], v[126:129] nt
	s_cbranch_vccnz .LBB0_226
	v_mul_f32_e32 v118, 0xbfb8aa3b, v118
	v_mul_f32_e32 v114, 0xbfb8aa3b, v114
	v_mul_f32_e32 v119, 0xbfb8aa3b, v119
	v_mul_f32_e32 v115, 0xbfb8aa3b, v115
	v_mul_f32_e32 v120, 0xbfb8aa3b, v120
	v_mul_f32_e32 v116, 0xbfb8aa3b, v116
	v_mul_f32_e32 v121, 0xbfb8aa3b, v121
	v_mul_f32_e32 v117, 0xbfb8aa3b, v117
	v_exp_f32_e32 v118, v118
	v_exp_f32_e32 v114, v114
	v_exp_f32_e32 v119, v119
	v_exp_f32_e32 v120, v120
	v_exp_f32_e32 v116, v116
	v_exp_f32_e32 v121, v121
	v_exp_f32_e32 v117, v117
	v_exp_f32_e32 v115, v115
	v_pk_add_f32 v[118:119], v[118:119], 1.0 op_sel_hi:[1,0]
	v_pk_add_f32 v[120:121], v[120:121], 1.0 op_sel_hi:[1,0]
	v_pk_add_f32 v[116:117], v[116:117], 1.0 op_sel_hi:[1,0]
	v_pk_add_f32 v[114:115], v[114:115], 1.0 op_sel_hi:[1,0]
.LBB0_226:
	s_and_b64 vcc, exec, s[38:39]
	v_cvt_pk_bf16_f32 v118, v118, v119
	v_cvt_pk_bf16_f32 v119, v120, v121
	v_cvt_pk_bf16_f32 v120, v114, v115
	v_cvt_pk_bf16_f32 v121, v116, v117
	flat_store_dwordx4 v[142:143], v[118:121] offset:256 nt
	s_cbranch_vccnz .LBB0_228
	v_mul_f32_e32 v110, 0xbfb8aa3b, v110
	v_mul_f32_e32 v106, 0xbfb8aa3b, v106
	v_mul_f32_e32 v111, 0xbfb8aa3b, v111
	v_mul_f32_e32 v107, 0xbfb8aa3b, v107
	v_mul_f32_e32 v112, 0xbfb8aa3b, v112
	v_mul_f32_e32 v108, 0xbfb8aa3b, v108
	v_mul_f32_e32 v113, 0xbfb8aa3b, v113
	v_mul_f32_e32 v109, 0xbfb8aa3b, v109
	v_exp_f32_e32 v110, v110
	v_exp_f32_e32 v106, v106
	v_exp_f32_e32 v111, v111
	v_exp_f32_e32 v112, v112
	v_exp_f32_e32 v108, v108
	v_exp_f32_e32 v113, v113
	v_exp_f32_e32 v109, v109
	v_exp_f32_e32 v107, v107
	v_pk_add_f32 v[110:111], v[110:111], 1.0 op_sel_hi:[1,0]
	v_pk_add_f32 v[112:113], v[112:113], 1.0 op_sel_hi:[1,0]
	v_pk_add_f32 v[108:109], v[108:109], 1.0 op_sel_hi:[1,0]
	v_pk_add_f32 v[106:107], v[106:107], 1.0 op_sel_hi:[1,0]
.LBB0_228:
	v_or_b32_e32 v116, 16, v148
	v_mov_b64_e32 v[114:115], s[2:3]
	v_mad_i64_i32 v[114:115], s[8:9], v116, s33, v[114:115]
	v_lshl_add_u64 v[114:115], v[140:141], 1, v[114:115]
	s_and_b64 vcc, exec, s[38:39]
	v_cvt_pk_bf16_f32 v110, v110, v111
	v_cvt_pk_bf16_f32 v111, v112, v113
	v_cvt_pk_bf16_f32 v112, v106, v107
	v_cvt_pk_bf16_f32 v113, v108, v109
	flat_store_dwordx4 v[114:115], v[110:113] nt
	s_cbranch_vccnz .LBB0_230
	v_mul_f32_e32 v102, 0xbfb8aa3b, v102
	v_mul_f32_e32 v98, 0xbfb8aa3b, v98
	v_mul_f32_e32 v103, 0xbfb8aa3b, v103
	v_mul_f32_e32 v99, 0xbfb8aa3b, v99
	v_mul_f32_e32 v104, 0xbfb8aa3b, v104
	v_mul_f32_e32 v100, 0xbfb8aa3b, v100
	v_mul_f32_e32 v105, 0xbfb8aa3b, v105
	v_mul_f32_e32 v101, 0xbfb8aa3b, v101
	v_exp_f32_e32 v102, v102
	v_exp_f32_e32 v98, v98
	v_exp_f32_e32 v103, v103
	v_exp_f32_e32 v104, v104
	v_exp_f32_e32 v100, v100
	v_exp_f32_e32 v105, v105
	v_exp_f32_e32 v101, v101
	v_exp_f32_e32 v99, v99
	v_pk_add_f32 v[102:103], v[102:103], 1.0 op_sel_hi:[1,0]
	v_pk_add_f32 v[104:105], v[104:105], 1.0 op_sel_hi:[1,0]
	v_pk_add_f32 v[100:101], v[100:101], 1.0 op_sel_hi:[1,0]
	v_pk_add_f32 v[98:99], v[98:99], 1.0 op_sel_hi:[1,0]
.LBB0_230:
	s_and_b64 vcc, exec, s[38:39]
	v_cvt_pk_bf16_f32 v102, v102, v103
	v_cvt_pk_bf16_f32 v103, v104, v105
	v_cvt_pk_bf16_f32 v104, v98, v99
	v_cvt_pk_bf16_f32 v105, v100, v101
	flat_store_dwordx4 v[114:115], v[102:105] offset:256 nt
	s_cbranch_vccnz .LBB0_232
	v_mul_f32_e32 v94, 0xbfb8aa3b, v94
	v_mul_f32_e32 v90, 0xbfb8aa3b, v90
	v_mul_f32_e32 v95, 0xbfb8aa3b, v95
	v_mul_f32_e32 v91, 0xbfb8aa3b, v91
	v_mul_f32_e32 v96, 0xbfb8aa3b, v96
	v_mul_f32_e32 v92, 0xbfb8aa3b, v92
	v_mul_f32_e32 v97, 0xbfb8aa3b, v97
	v_mul_f32_e32 v93, 0xbfb8aa3b, v93
	v_exp_f32_e32 v94, v94
	v_exp_f32_e32 v90, v90
	v_exp_f32_e32 v95, v95
	v_exp_f32_e32 v96, v96
	v_exp_f32_e32 v92, v92
	v_exp_f32_e32 v97, v97
	v_exp_f32_e32 v93, v93
	v_exp_f32_e32 v91, v91
	v_pk_add_f32 v[94:95], v[94:95], 1.0 op_sel_hi:[1,0]
	v_pk_add_f32 v[96:97], v[96:97], 1.0 op_sel_hi:[1,0]
	v_pk_add_f32 v[92:93], v[92:93], 1.0 op_sel_hi:[1,0]
	v_pk_add_f32 v[90:91], v[90:91], 1.0 op_sel_hi:[1,0]
.LBB0_232:
	v_or_b32_e32 v100, 32, v148
	v_mov_b64_e32 v[98:99], s[2:3]
	v_mad_i64_i32 v[98:99], s[8:9], v100, s33, v[98:99]
	v_lshl_add_u64 v[98:99], v[140:141], 1, v[98:99]
	s_and_b64 vcc, exec, s[38:39]
	v_cvt_pk_bf16_f32 v94, v94, v95
	v_cvt_pk_bf16_f32 v95, v96, v97
	v_cvt_pk_bf16_f32 v96, v90, v91
	v_cvt_pk_bf16_f32 v97, v92, v93
	flat_store_dwordx4 v[98:99], v[94:97] nt
	s_cbranch_vccnz .LBB0_234
	v_mul_f32_e32 v86, 0xbfb8aa3b, v86
	v_mul_f32_e32 v82, 0xbfb8aa3b, v82
	v_mul_f32_e32 v87, 0xbfb8aa3b, v87
	v_mul_f32_e32 v83, 0xbfb8aa3b, v83
	v_mul_f32_e32 v88, 0xbfb8aa3b, v88
	v_mul_f32_e32 v84, 0xbfb8aa3b, v84
	v_mul_f32_e32 v89, 0xbfb8aa3b, v89
	v_mul_f32_e32 v85, 0xbfb8aa3b, v85
	v_exp_f32_e32 v86, v86
	v_exp_f32_e32 v82, v82
	v_exp_f32_e32 v87, v87
	v_exp_f32_e32 v88, v88
	v_exp_f32_e32 v84, v84
	v_exp_f32_e32 v89, v89
	v_exp_f32_e32 v85, v85
	v_exp_f32_e32 v83, v83
	v_pk_add_f32 v[86:87], v[86:87], 1.0 op_sel_hi:[1,0]
	v_pk_add_f32 v[88:89], v[88:89], 1.0 op_sel_hi:[1,0]
	v_pk_add_f32 v[84:85], v[84:85], 1.0 op_sel_hi:[1,0]
	v_pk_add_f32 v[82:83], v[82:83], 1.0 op_sel_hi:[1,0]
; __device__ __forceinline__ unsigned cvt_pk_bf16(float lo, float hi) { unsigned r; asm volatile("v_cvt_pk_bf16_f32 %0, %1, %2" : "=v"(r) : "v"(lo), "v"(hi)); return r; }
;     __device__ __forceinline__ void operator()(const f32x4 (&acc)[2][2][4][2], const Unit& u, int wr, int wc, int fr, int fq) const {
;     ...
;         const int row0 = u.pm * BM + wr * 64 + fr; const int col0 = u.pn * BM + wc * 32 + 8 * fq; const bool sg = u.pn >= sig_pn;
; #pragma unroll
;         for (int ai = 0; ai < 2; ++ai)
; #pragma unroll
;             for (int m = 0; m < 4; ++m) { bf16* rowp = O + (size_t)(row0 + ai * HALF + m * 16) * ldc + col0;
; #pragma unroll
;                 for (int bj = 0; bj < 2; ++bj) { f32x4 v0 = acc[ai][bj][m][0], v1 = acc[ai][bj][m][1];
;                     if (sg) {
; #pragma unroll
;                         for (int j = 0; j < 4; ++j) { v0[j] = 1.0f + __expf(-v0[j]); v1[j] = 1.0f + __expf(-v1[j]); } }
;                     u32x4 w; w.x = cvt_pk_bf16(v0[0], v0[1]); w.y = cvt_pk_bf16(v0[2], v0[3]); w.z = cvt_pk_bf16(v1[0], v1[1]); w.w = cvt_pk_bf16(v1[2], v1[3]);
;                     *(u32x4*)(rowp + bj * HALF) = w; } }
.LBB0_234:
	s_and_b64 vcc, exec, s[38:39]
	v_cvt_pk_bf16_f32 v86, v86, v87
	v_cvt_pk_bf16_f32 v87, v88, v89
	v_cvt_pk_bf16_f32 v88, v82, v83
	v_cvt_pk_bf16_f32 v89, v84, v85
	flat_store_dwordx4 v[98:99], v[86:89] offset:256 nt
	s_cbranch_vccnz .LBB0_236
	v_mul_f32_e32 v78, 0xbfb8aa3b, v78
	v_mul_f32_e32 v74, 0xbfb8aa3b, v74
	v_mul_f32_e32 v79, 0xbfb8aa3b, v79
	v_mul_f32_e32 v75, 0xbfb8aa3b, v75
	v_mul_f32_e32 v80, 0xbfb8aa3b, v80
	v_mul_f32_e32 v76, 0xbfb8aa3b, v76
	v_mul_f32_e32 v81, 0xbfb8aa3b, v81
	v_mul_f32_e32 v77, 0xbfb8aa3b, v77
	v_exp_f32_e32 v78, v78
	v_exp_f32_e32 v74, v74
	v_exp_f32_e32 v79, v79
	v_exp_f32_e32 v80, v80
	v_exp_f32_e32 v76, v76
	v_exp_f32_e32 v81, v81
	v_exp_f32_e32 v77, v77
	v_exp_f32_e32 v75, v75
	v_pk_add_f32 v[78:79], v[78:79], 1.0 op_sel_hi:[1,0]
	v_pk_add_f32 v[80:81], v[80:81], 1.0 op_sel_hi:[1,0]
	v_pk_add_f32 v[76:77], v[76:77], 1.0 op_sel_hi:[1,0]
	v_pk_add_f32 v[74:75], v[74:75], 1.0 op_sel_hi:[1,0]
.LBB0_236:
	v_or_b32_e32 v84, 48, v148
	v_mov_b64_e32 v[82:83], s[2:3]
	v_mad_i64_i32 v[82:83], s[8:9], v84, s33, v[82:83]
	v_lshl_add_u64 v[82:83], v[140:141], 1, v[82:83]
	s_and_b64 vcc, exec, s[38:39]
	v_cvt_pk_bf16_f32 v78, v78, v79
	v_cvt_pk_bf16_f32 v79, v80, v81
	v_cvt_pk_bf16_f32 v80, v74, v75
	v_cvt_pk_bf16_f32 v81, v76, v77
	flat_store_dwordx4 v[82:83], v[78:81] nt
	s_cbranch_vccnz .LBB0_238
	v_mul_f32_e32 v70, 0xbfb8aa3b, v70
	v_mul_f32_e32 v66, 0xbfb8aa3b, v66
	v_mul_f32_e32 v71, 0xbfb8aa3b, v71
	v_mul_f32_e32 v67, 0xbfb8aa3b, v67
	v_mul_f32_e32 v72, 0xbfb8aa3b, v72
	v_mul_f32_e32 v68, 0xbfb8aa3b, v68
	v_mul_f32_e32 v73, 0xbfb8aa3b, v73
	v_mul_f32_e32 v69, 0xbfb8aa3b, v69
	v_exp_f32_e32 v70, v70
	v_exp_f32_e32 v66, v66
	v_exp_f32_e32 v71, v71
	v_exp_f32_e32 v72, v72
	v_exp_f32_e32 v68, v68
	v_exp_f32_e32 v73, v73
	v_exp_f32_e32 v69, v69
	v_exp_f32_e32 v67, v67
	v_pk_add_f32 v[70:71], v[70:71], 1.0 op_sel_hi:[1,0]
	v_pk_add_f32 v[72:73], v[72:73], 1.0 op_sel_hi:[1,0]
	v_pk_add_f32 v[68:69], v[68:69], 1.0 op_sel_hi:[1,0]
	v_pk_add_f32 v[66:67], v[66:67], 1.0 op_sel_hi:[1,0]
.LBB0_238:
	s_and_b64 vcc, exec, s[38:39]
	v_cvt_pk_bf16_f32 v70, v70, v71
	v_cvt_pk_bf16_f32 v71, v72, v73
	v_cvt_pk_bf16_f32 v72, v66, v67
	v_cvt_pk_bf16_f32 v73, v68, v69
	flat_store_dwordx4 v[82:83], v[70:73] offset:256 nt
	s_cbranch_vccnz .LBB0_240
	v_mul_f32_e32 v62, 0xbfb8aa3b, v62
	v_mul_f32_e32 v58, 0xbfb8aa3b, v58
	v_mul_f32_e32 v63, 0xbfb8aa3b, v63
	v_mul_f32_e32 v59, 0xbfb8aa3b, v59
	v_mul_f32_e32 v64, 0xbfb8aa3b, v64
	v_mul_f32_e32 v60, 0xbfb8aa3b, v60
	v_mul_f32_e32 v65, 0xbfb8aa3b, v65
	v_mul_f32_e32 v61, 0xbfb8aa3b, v61
	v_exp_f32_e32 v62, v62
	v_exp_f32_e32 v58, v58
	v_exp_f32_e32 v63, v63
	v_exp_f32_e32 v64, v64
	v_exp_f32_e32 v60, v60
	v_exp_f32_e32 v65, v65
	v_exp_f32_e32 v61, v61
	v_exp_f32_e32 v59, v59
	v_pk_add_f32 v[62:63], v[62:63], 1.0 op_sel_hi:[1,0]
	v_pk_add_f32 v[64:65], v[64:65], 1.0 op_sel_hi:[1,0]
	v_pk_add_f32 v[60:61], v[60:61], 1.0 op_sel_hi:[1,0]
	v_pk_add_f32 v[58:59], v[58:59], 1.0 op_sel_hi:[1,0]
.LBB0_240:
	v_add_u32_e32 v68, 0x80, v148
	v_mov_b64_e32 v[66:67], s[2:3]
	v_mad_i64_i32 v[66:67], s[8:9], v68, s33, v[66:67]
	v_lshl_add_u64 v[66:67], v[140:141], 1, v[66:67]
	s_and_b64 vcc, exec, s[38:39]
	v_cvt_pk_bf16_f32 v62, v62, v63
	v_cvt_pk_bf16_f32 v63, v64, v65
	v_cvt_pk_bf16_f32 v64, v58, v59
	v_cvt_pk_bf16_f32 v65, v60, v61
	flat_store_dwordx4 v[66:67], v[62:65] nt
	s_cbranch_vccnz .LBB0_242
	v_mul_f32_e32 v54, 0xbfb8aa3b, v54
	v_mul_f32_e32 v50, 0xbfb8aa3b, v50
	v_mul_f32_e32 v55, 0xbfb8aa3b, v55
	v_mul_f32_e32 v51, 0xbfb8aa3b, v51
	v_mul_f32_e32 v56, 0xbfb8aa3b, v56
	v_mul_f32_e32 v52, 0xbfb8aa3b, v52
	v_mul_f32_e32 v57, 0xbfb8aa3b, v57
	v_mul_f32_e32 v53, 0xbfb8aa3b, v53
	v_exp_f32_e32 v54, v54
	v_exp_f32_e32 v50, v50
	v_exp_f32_e32 v55, v55
	v_exp_f32_e32 v56, v56
	v_exp_f32_e32 v52, v52
	v_exp_f32_e32 v57, v57
	v_exp_f32_e32 v53, v53
	v_exp_f32_e32 v51, v51
	v_pk_add_f32 v[54:55], v[54:55], 1.0 op_sel_hi:[1,0]
	v_pk_add_f32 v[56:57], v[56:57], 1.0 op_sel_hi:[1,0]
	v_pk_add_f32 v[52:53], v[52:53], 1.0 op_sel_hi:[1,0]
	v_pk_add_f32 v[50:51], v[50:51], 1.0 op_sel_hi:[1,0]
.LBB0_242:
	s_and_b64 vcc, exec, s[38:39]
	v_cvt_pk_bf16_f32 v54, v54, v55
	v_cvt_pk_bf16_f32 v55, v56, v57
	v_cvt_pk_bf16_f32 v56, v50, v51
	v_cvt_pk_bf16_f32 v57, v52, v53
	flat_store_dwordx4 v[66:67], v[54:57] offset:256 nt
	s_cbranch_vccnz .LBB0_244
	v_mul_f32_e32 v46, 0xbfb8aa3b, v46
	v_mul_f32_e32 v42, 0xbfb8aa3b, v42
	v_mul_f32_e32 v47, 0xbfb8aa3b, v47
	v_mul_f32_e32 v43, 0xbfb8aa3b, v43
	v_mul_f32_e32 v48, 0xbfb8aa3b, v48
	v_mul_f32_e32 v44, 0xbfb8aa3b, v44
	v_mul_f32_e32 v49, 0xbfb8aa3b, v49
	v_mul_f32_e32 v45, 0xbfb8aa3b, v45
	v_exp_f32_e32 v46, v46
	v_exp_f32_e32 v42, v42
	v_exp_f32_e32 v47, v47
	v_exp_f32_e32 v48, v48
	v_exp_f32_e32 v44, v44
	v_exp_f32_e32 v49, v49
	v_exp_f32_e32 v45, v45
	v_exp_f32_e32 v43, v43
	v_pk_add_f32 v[46:47], v[46:47], 1.0 op_sel_hi:[1,0]
	v_pk_add_f32 v[48:49], v[48:49], 1.0 op_sel_hi:[1,0]
	v_pk_add_f32 v[44:45], v[44:45], 1.0 op_sel_hi:[1,0]
	v_pk_add_f32 v[42:43], v[42:43], 1.0 op_sel_hi:[1,0]
; __device__ __forceinline__ unsigned cvt_pk_bf16(float lo, float hi) { unsigned r; asm volatile("v_cvt_pk_bf16_f32 %0, %1, %2" : "=v"(r) : "v"(lo), "v"(hi)); return r; }
;     __device__ __forceinline__ void operator()(const f32x4 (&acc)[2][2][4][2], const Unit& u, int wr, int wc, int fr, int fq) const {
;     ...
;         const int row0 = u.pm * BM + wr * 64 + fr; const int col0 = u.pn * BM + wc * 32 + 8 * fq; const bool sg = u.pn >= sig_pn;
; #pragma unroll
;         for (int ai = 0; ai < 2; ++ai)
; #pragma unroll
;             for (int m = 0; m < 4; ++m) { bf16* rowp = O + (size_t)(row0 + ai * HALF + m * 16) * ldc + col0;
; #pragma unroll
;                 for (int bj = 0; bj < 2; ++bj) { f32x4 v0 = acc[ai][bj][m][0], v1 = acc[ai][bj][m][1];
;                     if (sg) {
; #pragma unroll
;                         for (int j = 0; j < 4; ++j) { v0[j] = 1.0f + __expf(-v0[j]); v1[j] = 1.0f + __expf(-v1[j]); } }
;                     u32x4 w; w.x = cvt_pk_bf16(v0[0], v0[1]); w.y = cvt_pk_bf16(v0[2], v0[3]); w.z = cvt_pk_bf16(v1[0], v1[1]); w.w = cvt_pk_bf16(v1[2], v1[3]);
;                     *(u32x4*)(rowp + bj * HALF) = w; } }
.LBB0_244:
	v_add_u32_e32 v52, 0x90, v148
	v_mov_b64_e32 v[50:51], s[2:3]
	v_mad_i64_i32 v[50:51], s[8:9], v52, s33, v[50:51]
	v_lshl_add_u64 v[50:51], v[140:141], 1, v[50:51]
	s_and_b64 vcc, exec, s[38:39]
	v_cvt_pk_bf16_f32 v46, v46, v47
	v_cvt_pk_bf16_f32 v47, v48, v49
	v_cvt_pk_bf16_f32 v48, v42, v43
	v_cvt_pk_bf16_f32 v49, v44, v45
	flat_store_dwordx4 v[50:51], v[46:49] nt
	s_cbranch_vccnz .LBB0_246
	v_mul_f32_e32 v38, 0xbfb8aa3b, v38
	v_mul_f32_e32 v34, 0xbfb8aa3b, v34
	v_mul_f32_e32 v39, 0xbfb8aa3b, v39
	v_mul_f32_e32 v35, 0xbfb8aa3b, v35
	v_mul_f32_e32 v40, 0xbfb8aa3b, v40
	v_mul_f32_e32 v36, 0xbfb8aa3b, v36
	v_mul_f32_e32 v41, 0xbfb8aa3b, v41
	v_mul_f32_e32 v37, 0xbfb8aa3b, v37
	v_exp_f32_e32 v38, v38
	v_exp_f32_e32 v34, v34
	v_exp_f32_e32 v39, v39
	v_exp_f32_e32 v40, v40
	v_exp_f32_e32 v36, v36
	v_exp_f32_e32 v41, v41
	v_exp_f32_e32 v37, v37
	v_exp_f32_e32 v35, v35
	v_pk_add_f32 v[38:39], v[38:39], 1.0 op_sel_hi:[1,0]
	v_pk_add_f32 v[40:41], v[40:41], 1.0 op_sel_hi:[1,0]
	v_pk_add_f32 v[36:37], v[36:37], 1.0 op_sel_hi:[1,0]
	v_pk_add_f32 v[34:35], v[34:35], 1.0 op_sel_hi:[1,0]
.LBB0_246:
	s_and_b64 vcc, exec, s[38:39]
	v_cvt_pk_bf16_f32 v38, v38, v39
	v_cvt_pk_bf16_f32 v39, v40, v41
	v_cvt_pk_bf16_f32 v40, v34, v35
	v_cvt_pk_bf16_f32 v41, v36, v37
	flat_store_dwordx4 v[50:51], v[38:41] offset:256 nt
	s_cbranch_vccnz .LBB0_248
	v_mul_f32_e32 v30, 0xbfb8aa3b, v30
	v_mul_f32_e32 v26, 0xbfb8aa3b, v26
	v_mul_f32_e32 v31, 0xbfb8aa3b, v31
	v_mul_f32_e32 v27, 0xbfb8aa3b, v27
	v_mul_f32_e32 v32, 0xbfb8aa3b, v32
	v_mul_f32_e32 v28, 0xbfb8aa3b, v28
	v_mul_f32_e32 v33, 0xbfb8aa3b, v33
	v_mul_f32_e32 v29, 0xbfb8aa3b, v29
	v_exp_f32_e32 v30, v30
	v_exp_f32_e32 v26, v26
	v_exp_f32_e32 v31, v31
	v_exp_f32_e32 v32, v32
	v_exp_f32_e32 v28, v28
	v_exp_f32_e32 v33, v33
	v_exp_f32_e32 v29, v29
	v_exp_f32_e32 v27, v27
	v_pk_add_f32 v[30:31], v[30:31], 1.0 op_sel_hi:[1,0]
	v_pk_add_f32 v[32:33], v[32:33], 1.0 op_sel_hi:[1,0]
	v_pk_add_f32 v[28:29], v[28:29], 1.0 op_sel_hi:[1,0]
	v_pk_add_f32 v[26:27], v[26:27], 1.0 op_sel_hi:[1,0]
.LBB0_248:
	v_add_u32_e32 v36, 0xa0, v148
	v_mov_b64_e32 v[34:35], s[2:3]
	v_mad_i64_i32 v[34:35], s[8:9], v36, s33, v[34:35]
	v_lshl_add_u64 v[34:35], v[140:141], 1, v[34:35]
	s_and_b64 vcc, exec, s[38:39]
	v_cvt_pk_bf16_f32 v30, v30, v31
	v_cvt_pk_bf16_f32 v31, v32, v33
	v_cvt_pk_bf16_f32 v32, v26, v27
	v_cvt_pk_bf16_f32 v33, v28, v29
	flat_store_dwordx4 v[34:35], v[30:33] nt
	s_cbranch_vccnz .LBB0_250
	v_mul_f32_e32 v22, 0xbfb8aa3b, v22
	v_mul_f32_e32 v18, 0xbfb8aa3b, v18
	v_mul_f32_e32 v23, 0xbfb8aa3b, v23
	v_mul_f32_e32 v19, 0xbfb8aa3b, v19
	v_mul_f32_e32 v24, 0xbfb8aa3b, v24
	v_mul_f32_e32 v20, 0xbfb8aa3b, v20
	v_mul_f32_e32 v25, 0xbfb8aa3b, v25
	v_mul_f32_e32 v21, 0xbfb8aa3b, v21
	v_exp_f32_e32 v22, v22
	v_exp_f32_e32 v18, v18
	v_exp_f32_e32 v23, v23
	v_exp_f32_e32 v24, v24
	v_exp_f32_e32 v20, v20
	v_exp_f32_e32 v25, v25
	v_exp_f32_e32 v21, v21
	v_exp_f32_e32 v19, v19
	v_pk_add_f32 v[22:23], v[22:23], 1.0 op_sel_hi:[1,0]
	v_pk_add_f32 v[24:25], v[24:25], 1.0 op_sel_hi:[1,0]
	v_pk_add_f32 v[20:21], v[20:21], 1.0 op_sel_hi:[1,0]
	v_pk_add_f32 v[18:19], v[18:19], 1.0 op_sel_hi:[1,0]
.LBB0_250:
	s_and_b64 vcc, exec, s[38:39]
	v_cvt_pk_bf16_f32 v22, v22, v23
	v_cvt_pk_bf16_f32 v23, v24, v25
	v_cvt_pk_bf16_f32 v24, v18, v19
	v_cvt_pk_bf16_f32 v25, v20, v21
	flat_store_dwordx4 v[34:35], v[22:25] offset:256 nt
	s_cbranch_vccnz .LBB0_252
	v_mul_f32_e32 v14, 0xbfb8aa3b, v14
	v_mul_f32_e32 v10, 0xbfb8aa3b, v10
	v_mul_f32_e32 v15, 0xbfb8aa3b, v15
	v_mul_f32_e32 v11, 0xbfb8aa3b, v11
	v_mul_f32_e32 v16, 0xbfb8aa3b, v16
	v_mul_f32_e32 v12, 0xbfb8aa3b, v12
	v_mul_f32_e32 v17, 0xbfb8aa3b, v17
	v_mul_f32_e32 v13, 0xbfb8aa3b, v13
	v_exp_f32_e32 v14, v14
	v_exp_f32_e32 v10, v10
	v_exp_f32_e32 v15, v15
	v_exp_f32_e32 v16, v16
	v_exp_f32_e32 v12, v12
	v_exp_f32_e32 v17, v17
	v_exp_f32_e32 v13, v13
	v_exp_f32_e32 v11, v11
	v_pk_add_f32 v[14:15], v[14:15], 1.0 op_sel_hi:[1,0]
	v_pk_add_f32 v[16:17], v[16:17], 1.0 op_sel_hi:[1,0]
	v_pk_add_f32 v[12:13], v[12:13], 1.0 op_sel_hi:[1,0]
	v_pk_add_f32 v[10:11], v[10:11], 1.0 op_sel_hi:[1,0]
.LBB0_252:
	v_add_u32_e32 v20, 0xb0, v148
	v_mov_b64_e32 v[18:19], s[2:3]
	v_mad_i64_i32 v[18:19], s[8:9], v20, s33, v[18:19]
	v_lshl_add_u64 v[18:19], v[140:141], 1, v[18:19]
	s_and_b64 vcc, exec, s[38:39]
	v_cvt_pk_bf16_f32 v14, v14, v15
	v_cvt_pk_bf16_f32 v15, v16, v17
	v_cvt_pk_bf16_f32 v16, v10, v11
	v_cvt_pk_bf16_f32 v17, v12, v13
	flat_store_dwordx4 v[18:19], v[14:17] nt
	s_cbranch_vccnz .LBB0_254
	v_mul_f32_e32 v6, 0xbfb8aa3b, v6
	v_mul_f32_e32 v2, 0xbfb8aa3b, v2
	v_mul_f32_e32 v7, 0xbfb8aa3b, v7
	v_mul_f32_e32 v3, 0xbfb8aa3b, v3
	v_mul_f32_e32 v8, 0xbfb8aa3b, v8
	v_mul_f32_e32 v4, 0xbfb8aa3b, v4
	v_mul_f32_e32 v9, 0xbfb8aa3b, v9
	v_mul_f32_e32 v5, 0xbfb8aa3b, v5
	v_exp_f32_e32 v6, v6
	v_exp_f32_e32 v2, v2
	v_exp_f32_e32 v7, v7
	v_exp_f32_e32 v8, v8
	v_exp_f32_e32 v4, v4
	v_exp_f32_e32 v9, v9
	v_exp_f32_e32 v5, v5
	v_exp_f32_e32 v3, v3
	v_pk_add_f32 v[6:7], v[6:7], 1.0 op_sel_hi:[1,0]
	v_pk_add_f32 v[8:9], v[8:9], 1.0 op_sel_hi:[1,0]
	v_pk_add_f32 v[4:5], v[4:5], 1.0 op_sel_hi:[1,0]
	v_pk_add_f32 v[2:3], v[2:3], 1.0 op_sel_hi:[1,0]
.LBB0_254:
	s_andn2_b64 vcc, exec, s[42:43]
	s_mov_b64 s[38:39], -1
	v_cvt_pk_bf16_f32 v6, v6, v7
	v_cvt_pk_bf16_f32 v7, v8, v9
	v_cvt_pk_bf16_f32 v8, v2, v3
	v_cvt_pk_bf16_f32 v9, v4, v5
	flat_store_dwordx4 v[18:19], v[6:9] offset:256 nt
	s_cbranch_vccnz .LBB0_214
	s_andn2_b64 vcc, exec, s[0:1]
	s_cbranch_vccnz .LBB0_213
	s_barrier
	s_branch .LBB0_213
